# v14 + nt on the P0 f32 weight loads (adaLN GEMV weights and the dense-weight conversion reads)
# speedup vs baseline: 1.0215x; 1.0215x over previous
.LBB0_14:
	global_load_dwordx4 v[10:13], v19, s[20:21] offset:-28
	global_load_dwordx4 v[2:5], v19, s[20:21] offset:-12
	v_lshl_add_u64 v[16:17], v[14:15], 0, s[22:23]
	v_add_co_u32_e32 v54, vcc, s28, v16
	s_add_u32 s22, s22, 0x60000
	s_nop 0
	v_addc_co_u32_e32 v55, vcc, 0, v17, vcc
	v_add_co_u32_e32 v56, vcc, s29, v16
	s_addc_u32 s23, s23, 0
	s_nop 0
	v_addc_co_u32_e32 v57, vcc, 0, v17, vcc
	v_add_co_u32_e32 v58, vcc, s30, v16
	s_add_u32 s20, s20, 32
	s_nop 0
	v_addc_co_u32_e32 v59, vcc, 0, v17, vcc
	v_add_co_u32_e32 v60, vcc, s31, v16
	s_addc_u32 s21, s21, 0
	s_nop 0
	v_addc_co_u32_e32 v61, vcc, 0, v17, vcc
	v_add_co_u32_e32 v62, vcc, s33, v16
	s_cmp_eq_u32 s22, 0x180000
	s_nop 0
	v_addc_co_u32_e32 v63, vcc, 0, v17, vcc
	v_add_co_u32_e32 v64, vcc, s34, v16
	s_waitcnt vmcnt(1)
	v_mul_f32_e32 v21, 0xbfb8aa3b, v12
	v_addc_co_u32_e32 v65, vcc, 0, v17, vcc
	v_add_co_u32_e32 v66, vcc, s35, v16
	v_exp_f32_e32 v21, v21
	s_nop 0
	v_addc_co_u32_e32 v67, vcc, 0, v17, vcc
	global_load_dwordx4 v[22:25], v[16:17], off nt
	global_load_dwordx4 v[26:29], v[54:55], off nt
	global_load_dwordx4 v[30:33], v[56:57], off nt
	global_load_dwordx4 v[34:37], v[58:59], off nt
	global_load_dwordx4 v[38:41], v[60:61], off nt
	global_load_dwordx4 v[42:45], v[62:63], off nt
	global_load_dwordx4 v[46:49], v[64:65], off nt
	global_load_dwordx4 v[50:53], v[66:67], off nt
	v_mul_f32_e32 v16, 0xbfb8aa3b, v10
	v_mul_f32_e32 v17, 0xbfb8aa3b, v11
	v_exp_f32_e32 v16, v16
	v_exp_f32_e32 v17, v17
	v_mul_f32_e32 v54, 0xbfb8aa3b, v13
	s_waitcnt vmcnt(8)
	v_mul_f32_e32 v55, 0xbfb8aa3b, v2
	v_exp_f32_e32 v54, v54
	v_mul_f32_e32 v56, 0xbfb8aa3b, v3
	v_exp_f32_e32 v55, v55
	v_add_f32_e32 v16, 1.0, v16
	v_mul_f32_e32 v57, 0xbfb8aa3b, v4
	v_exp_f32_e32 v56, v56
	v_add_f32_e32 v17, 1.0, v17
	v_div_scale_f32 v59, s[2:3], v16, v16, v10
	v_mul_f32_e32 v58, 0xbfb8aa3b, v5
	v_exp_f32_e32 v57, v57
	v_add_f32_e32 v21, 1.0, v21
	v_div_scale_f32 v61, s[2:3], v17, v17, v11
	v_rcp_f32_e32 v75, v59
	v_exp_f32_e32 v58, v58
	v_add_f32_e32 v54, 1.0, v54
	v_div_scale_f32 v63, s[4:5], v21, v21, v12
	v_rcp_f32_e32 v76, v61
	v_add_f32_e32 v55, 1.0, v55
	v_div_scale_f32 v65, s[6:7], v54, v54, v13
	v_rcp_f32_e32 v77, v63
	v_add_f32_e32 v56, 1.0, v56
	v_div_scale_f32 v67, s[8:9], v55, v55, v2
	v_rcp_f32_e32 v78, v65
	v_add_f32_e32 v57, 1.0, v57
	v_div_scale_f32 v69, s[10:11], v56, v56, v3
	v_rcp_f32_e32 v79, v67
	v_fma_f32 v83, -v59, v75, 1.0
	v_add_f32_e32 v58, 1.0, v58
	v_div_scale_f32 v60, vcc, v10, v16, v10
	v_div_scale_f32 v71, s[12:13], v57, v57, v4
	v_rcp_f32_e32 v80, v69
	v_fma_f32 v84, -v61, v76, 1.0
	v_fmac_f32_e32 v75, v83, v75
	v_div_scale_f32 v62, s[2:3], v11, v17, v11
	v_div_scale_f32 v73, s[14:15], v58, v58, v5
	v_rcp_f32_e32 v81, v71
	v_fma_f32 v85, -v63, v77, 1.0
	v_fmac_f32_e32 v76, v84, v76
	v_mul_f32_e32 v83, v60, v75
	v_div_scale_f32 v64, s[4:5], v12, v21, v12
	v_rcp_f32_e32 v82, v73
	v_fma_f32 v86, -v65, v78, 1.0
	v_fmac_f32_e32 v77, v85, v77
	v_mul_f32_e32 v84, v62, v76
	v_fma_f32 v91, -v59, v83, v60
	v_div_scale_f32 v66, s[6:7], v13, v54, v13
	v_fma_f32 v87, -v67, v79, 1.0
	v_fmac_f32_e32 v78, v86, v78
	v_mul_f32_e32 v85, v64, v77
	v_fma_f32 v92, -v61, v84, v62
	v_fmac_f32_e32 v83, v91, v75
	v_div_scale_f32 v68, s[8:9], v2, v55, v2
	v_fma_f32 v88, -v69, v80, 1.0
	v_fmac_f32_e32 v79, v87, v79
	v_mul_f32_e32 v86, v66, v78
	v_fma_f32 v93, -v63, v85, v64
	v_fmac_f32_e32 v84, v92, v76
	v_fma_f32 v59, -v59, v83, v60
	v_div_scale_f32 v70, s[10:11], v3, v56, v3
	v_fma_f32 v89, -v71, v81, 1.0
	v_fmac_f32_e32 v80, v88, v80
	v_mul_f32_e32 v87, v68, v79
	v_fma_f32 v94, -v65, v86, v66
	v_fmac_f32_e32 v85, v93, v77
	v_fma_f32 v60, -v61, v84, v62
	v_div_fmas_f32 v59, v59, v75, v83
	s_mov_b64 vcc, s[2:3]
	v_div_scale_f32 v72, s[12:13], v4, v57, v4
	v_fma_f32 v90, -v73, v82, 1.0
	v_fmac_f32_e32 v81, v89, v81
	v_mul_f32_e32 v88, v70, v80
	v_fma_f32 v95, -v67, v87, v68
	v_fmac_f32_e32 v86, v94, v78
	v_fma_f32 v61, -v63, v85, v64
	v_div_fixup_f32 v10, v59, v16, v10
	v_div_fmas_f32 v16, v60, v76, v84
	s_mov_b64 vcc, s[4:5]
	v_div_scale_f32 v74, s[14:15], v5, v58, v5
	v_fmac_f32_e32 v82, v90, v82
	v_mul_f32_e32 v89, v72, v81
	v_fma_f32 v96, -v69, v88, v70
	v_fmac_f32_e32 v87, v95, v79
	v_fma_f32 v62, -v65, v86, v66
	s_waitcnt vmcnt(7)
	v_pk_fma_f32 v[6:7], v[22:23], v[10:11], v[6:7] op_sel_hi:[1,0,1]
	v_pk_fma_f32 v[8:9], v[24:25], v[10:11], v[8:9] op_sel_hi:[1,0,1]
	v_div_fixup_f32 v10, v16, v17, v11
	v_div_fmas_f32 v11, v61, v77, v85
	s_mov_b64 vcc, s[6:7]
	v_mul_f32_e32 v90, v74, v82
	v_fma_f32 v97, -v71, v89, v72
	v_fmac_f32_e32 v88, v96, v80
	v_fma_f32 v63, -v67, v87, v68
	s_waitcnt vmcnt(6)
	v_pk_fma_f32 v[8:9], v[28:29], v[10:11], v[8:9] op_sel_hi:[1,0,1]
	v_pk_fma_f32 v[6:7], v[26:27], v[10:11], v[6:7] op_sel_hi:[1,0,1]
	v_div_fmas_f32 v16, v62, v78, v86
	v_div_fixup_f32 v10, v11, v21, v12
	s_mov_b64 vcc, s[8:9]
	v_fma_f32 v98, -v73, v90, v74
	v_fmac_f32_e32 v89, v97, v81
	v_fma_f32 v64, -v69, v88, v70
	s_waitcnt vmcnt(5)
	v_pk_fma_f32 v[6:7], v[30:31], v[10:11], v[6:7] op_sel_hi:[1,0,1]
	v_pk_fma_f32 v[8:9], v[32:33], v[10:11], v[8:9] op_sel_hi:[1,0,1]
	v_div_fixup_f32 v10, v16, v54, v13
	v_div_fmas_f32 v11, v63, v79, v87
	s_mov_b64 vcc, s[10:11]
	v_fmac_f32_e32 v90, v98, v82
	v_fma_f32 v65, -v71, v89, v72
	s_waitcnt vmcnt(4)
	v_pk_fma_f32 v[8:9], v[36:37], v[10:11], v[8:9] op_sel_hi:[1,0,1]
	v_pk_fma_f32 v[6:7], v[34:35], v[10:11], v[6:7] op_sel_hi:[1,0,1]
	v_div_fixup_f32 v2, v11, v55, v2
	v_div_fmas_f32 v10, v64, v80, v88
	s_mov_b64 vcc, s[12:13]
	v_fma_f32 v66, -v73, v90, v74
	s_waitcnt vmcnt(3)
	v_pk_fma_f32 v[6:7], v[38:39], v[2:3], v[6:7] op_sel_hi:[1,0,1]
	v_pk_fma_f32 v[8:9], v[40:41], v[2:3], v[8:9] op_sel_hi:[1,0,1]
	v_div_fixup_f32 v2, v10, v56, v3
	v_div_fmas_f32 v10, v65, v81, v89
	s_mov_b64 vcc, s[14:15]
	s_waitcnt vmcnt(2)
	v_pk_fma_f32 v[8:9], v[44:45], v[2:3], v[8:9] op_sel_hi:[1,0,1]
	v_pk_fma_f32 v[2:3], v[42:43], v[2:3], v[6:7] op_sel_hi:[1,0,1]
	v_div_fixup_f32 v4, v10, v57, v4
	v_div_fmas_f32 v10, v66, v82, v90
	s_waitcnt vmcnt(1)
	v_pk_fma_f32 v[2:3], v[46:47], v[4:5], v[2:3] op_sel_hi:[1,0,1]
	v_pk_fma_f32 v[6:7], v[48:49], v[4:5], v[8:9] op_sel_hi:[1,0,1]
	v_div_fixup_f32 v4, v10, v58, v5
	s_waitcnt vmcnt(0)
	v_pk_fma_f32 v[8:9], v[52:53], v[4:5], v[6:7] op_sel_hi:[1,0,1]
	v_pk_fma_f32 v[6:7], v[50:51], v[4:5], v[2:3] op_sel_hi:[1,0,1]
	s_cbranch_scc0 .LBB0_14
	ds_write_b128 v20, v[6:9]
	s_waitcnt lgkmcnt(0)
	s_barrier
	s_and_saveexec_b64 s[2:3], s[0:1]
	s_cbranch_execz .LBB0_12
	ds_read2st64_b32 v[2:3], v18 offset1:4
	ds_read2st64_b32 v[4:5], v18 offset0:8 offset1:12
	ds_read2st64_b32 v[6:7], v18 offset0:16 offset1:20
	ds_read2st64_b32 v[8:9], v18 offset0:24 offset1:28
	s_mul_i32 s4, s38, 0x3000
	s_waitcnt lgkmcnt(3)
	v_add_f32_e32 v2, 0, v2
	v_add_f32_e32 v2, v2, v3
	s_waitcnt lgkmcnt(2)
	v_add_f32_e32 v2, v2, v4
	v_add_f32_e32 v2, v2, v5
	s_waitcnt lgkmcnt(1)
	v_add_f32_e32 v2, v2, v6
	v_add_f32_e32 v2, v2, v7
	s_waitcnt lgkmcnt(0)
	v_add_f32_e32 v2, v2, v8
	s_add_i32 s4, s4, s37
	v_add_f32_e32 v4, v2, v9
	v_or_b32_e32 v2, s4, v0
	v_ashrrev_i32_e32 v3, 31, v2
	v_lshl_add_u64 v[2:3], v[2:3], 2, s[18:19]
	global_store_dword v[2:3], v4, off
	s_branch .LBB0_12

.LBB0_41:
	v_lshrrev_b32_e32 v1, 4, v196
	v_lshlrev_b32_e32 v2, 2, v0
	v_and_b32_e32 v130, 60, v2
	v_mul_u32_u24_e32 v2, s4, v1
	v_mov_b32_e32 v133, 0
	v_lshlrev_b32_e32 v132, 2, v2
	v_lshl_add_u64 v[2:3], s[2:3], 0, v[132:133]
	v_lshlrev_b32_e32 v132, 2, v130
	v_or_b32_e32 v131, 4, v1
	v_lshl_add_u64 v[10:11], v[2:3], 0, v[132:133]
	v_mul_u32_u24_e32 v2, s4, v131
	v_lshlrev_b32_e32 v2, 2, v2
	v_mov_b32_e32 v3, v133
	v_lshl_add_u64 v[2:3], s[2:3], 0, v[2:3]
	v_or_b32_e32 v135, 8, v1
	v_lshl_add_u64 v[12:13], v[2:3], 0, v[132:133]
	global_load_dwordx4 v[2:5], v[10:11], off nt
	global_load_dwordx4 v[6:9], v[12:13], off nt
	v_mul_u32_u24_e32 v10, s4, v135
	v_lshlrev_b32_e32 v10, 2, v10
	v_mov_b32_e32 v11, v133
	v_lshl_add_u64 v[10:11], s[2:3], 0, v[10:11]
	v_or_b32_e32 v139, 12, v1
	v_lshl_add_u64 v[42:43], v[10:11], 0, v[132:133]
	v_mul_u32_u24_e32 v10, s4, v139
	v_lshlrev_b32_e32 v10, 2, v10
	v_mov_b32_e32 v11, v133
	v_lshl_add_u64 v[10:11], s[2:3], 0, v[10:11]
	v_or_b32_e32 v141, 16, v1
	v_lshl_add_u64 v[44:45], v[10:11], 0, v[132:133]
	v_mul_u32_u24_e32 v10, s4, v141
	v_lshlrev_b32_e32 v10, 2, v10
	v_mov_b32_e32 v11, v133
	v_lshl_add_u64 v[10:11], s[2:3], 0, v[10:11]
	v_or_b32_e32 v143, 20, v1
	v_lshl_add_u64 v[46:47], v[10:11], 0, v[132:133]
	v_mul_u32_u24_e32 v10, s4, v143
	v_lshlrev_b32_e32 v10, 2, v10
	v_mov_b32_e32 v11, v133
	v_lshl_add_u64 v[10:11], s[2:3], 0, v[10:11]
	v_or_b32_e32 v145, 24, v1
	v_lshl_add_u64 v[48:49], v[10:11], 0, v[132:133]
	v_mul_u32_u24_e32 v10, s4, v145
	v_lshlrev_b32_e32 v10, 2, v10
	v_mov_b32_e32 v11, v133
	v_lshl_add_u64 v[10:11], s[2:3], 0, v[10:11]
	v_or_b32_e32 v147, 28, v1
	v_lshl_add_u64 v[58:59], v[10:11], 0, v[132:133]
	v_mul_u32_u24_e32 v10, s4, v147
	v_lshlrev_b32_e32 v10, 2, v10
	v_mov_b32_e32 v11, v133
	v_lshl_add_u64 v[10:11], s[2:3], 0, v[10:11]
	v_or_b32_e32 v149, 32, v1
	v_lshl_add_u64 v[60:61], v[10:11], 0, v[132:133]
	v_mul_u32_u24_e32 v10, s4, v149
	v_lshlrev_b32_e32 v10, 2, v10
	v_mov_b32_e32 v11, v133
	v_lshl_add_u64 v[10:11], s[2:3], 0, v[10:11]
	v_or_b32_e32 v151, 36, v1
	v_lshl_add_u64 v[62:63], v[10:11], 0, v[132:133]
	v_mul_u32_u24_e32 v10, s4, v151
	v_lshlrev_b32_e32 v10, 2, v10
	v_mov_b32_e32 v11, v133
	v_lshl_add_u64 v[10:11], s[2:3], 0, v[10:11]
	v_or_b32_e32 v154, 40, v1
	v_lshl_add_u64 v[64:65], v[10:11], 0, v[132:133]
	v_mul_u32_u24_e32 v10, s4, v154
	v_lshlrev_b32_e32 v10, 2, v10
	v_mov_b32_e32 v11, v133
	v_lshl_add_u64 v[10:11], s[2:3], 0, v[10:11]
	v_or_b32_e32 v155, 44, v1
	v_lshl_add_u64 v[74:75], v[10:11], 0, v[132:133]
	v_mul_u32_u24_e32 v10, s4, v155
	v_lshlrev_b32_e32 v10, 2, v10
	v_mov_b32_e32 v11, v133
	v_lshl_add_u64 v[10:11], s[2:3], 0, v[10:11]
	v_or_b32_e32 v156, 48, v1
	v_lshl_add_u64 v[76:77], v[10:11], 0, v[132:133]
	v_mul_u32_u24_e32 v10, s4, v156
	v_lshlrev_b32_e32 v10, 2, v10
	v_mov_b32_e32 v11, v133
	v_lshl_add_u64 v[10:11], s[2:3], 0, v[10:11]
	v_or_b32_e32 v157, 52, v1
	v_lshl_add_u64 v[78:79], v[10:11], 0, v[132:133]
	v_mul_u32_u24_e32 v10, s4, v157
	v_lshlrev_b32_e32 v10, 2, v10
	v_mov_b32_e32 v11, v133
	v_lshl_add_u64 v[10:11], s[2:3], 0, v[10:11]
	v_or_b32_e32 v158, 56, v1
	v_lshl_add_u64 v[80:81], v[10:11], 0, v[132:133]
	v_mul_u32_u24_e32 v10, s4, v158
	v_lshlrev_b32_e32 v10, 2, v10
	v_mov_b32_e32 v11, v133
	v_lshl_add_u64 v[10:11], s[2:3], 0, v[10:11]
	v_or_b32_e32 v159, 60, v1
	v_lshl_add_u64 v[90:91], v[10:11], 0, v[132:133]
	v_mul_u32_u24_e32 v10, s4, v159
	v_lshlrev_b32_e32 v10, 2, v10
	v_mov_b32_e32 v11, v133
	v_lshl_add_u64 v[10:11], s[2:3], 0, v[10:11]
	v_lshl_add_u64 v[92:93], v[10:11], 0, v[132:133]
	global_load_dwordx4 v[10:13], v[42:43], off nt
	global_load_dwordx4 v[14:17], v[44:45], off nt
	global_load_dwordx4 v[18:21], v[46:47], off nt
	global_load_dwordx4 v[22:25], v[48:49], off nt
	global_load_dwordx4 v[26:29], v[58:59], off nt
	global_load_dwordx4 v[30:33], v[60:61], off nt
	global_load_dwordx4 v[34:37], v[62:63], off nt
	global_load_dwordx4 v[38:41], v[64:65], off nt
	global_load_dwordx4 v[50:53], v[74:75], off nt
	global_load_dwordx4 v[54:57], v[76:77], off nt
	global_load_dwordx4 v[66:69], v[78:79], off nt
	global_load_dwordx4 v[70:73], v[80:81], off nt
	global_load_dwordx4 v[82:85], v[90:91], off nt
	global_load_dwordx4 v[86:89], v[92:93], off nt
	s_mul_i32 s2, s88, 0x4100
	s_lshl_b32 s11, s52, 3
	s_add_i32 s2, s2, 0
	s_add_u32 s12, s50, 0x1600000
	s_addc_u32 s13, s51, 0
	s_add_u32 s14, s50, 0xe00000
	s_addc_u32 s15, s51, 0
	s_add_u32 s18, s50, 0xa00000
	s_addc_u32 s19, s51, 0
	v_and_b32_e32 v44, 7, v0
	v_lshrrev_b32_e32 v134, 3, v196
	v_add_u32_e32 v42, s2, v132
	v_mul_u32_u24_e32 v43, 0x104, v1
	s_add_u32 s20, s50, 0xd200000
	v_lshlrev_b32_e32 v136, 3, v44
	v_mul_u32_u24_e32 v44, 0x820, v44
	v_lshlrev_b32_e32 v45, 2, v134
	s_addc_u32 s21, s51, 0
	v_mov_b32_e32 v137, v133
	v_add3_u32 v160, s2, v44, v45
	s_add_i32 s22, 0, 0x27e60
	s_add_i32 s23, 0, 0x27e58
	s_add_i32 s24, 0, 0x27e50
	s_add_i32 s25, 0, 0x27e30
	s_mov_b32 s26, 0xc3e00000
	v_add_u32_e32 v161, v42, v43
	v_mov_b32_e32 v162, 0x43e00000
	s_mov_b32 s28, s10
	s_mov_b64 s[2:3], s[0:1]
	v_or_b32_e32 v138, 8, v134
	v_or_b32_e32 v140, 16, v134
	v_or_b32_e32 v142, 24, v134
	v_or_b32_e32 v144, 32, v134
	v_or_b32_e32 v146, 40, v134
	v_or_b32_e32 v148, 48, v134
	v_or_b32_e32 v150, 56, v134
	s_branch .LBB0_45
.LBB0_42:
	v_mul_u32_u24_e32 v2, s8, v1
	v_mul_u32_u24_e32 v4, s8, v131
	v_mul_u32_u24_e32 v10, s8, v135
	v_mul_u32_u24_e32 v12, s8, v139
	v_mul_u32_u24_e32 v18, s8, v141
	v_mul_u32_u24_e32 v20, s8, v143
	v_mul_u32_u24_e32 v26, s8, v145
	v_mul_u32_u24_e32 v28, s8, v147
	v_mul_u32_u24_e32 v34, s8, v149
	v_mul_u32_u24_e32 v36, s8, v151
	v_mul_u32_u24_e32 v50, s8, v154
	v_mul_u32_u24_e32 v52, s8, v155
	v_mul_u32_u24_e32 v66, s8, v156
	v_mul_u32_u24_e32 v68, s8, v157
	v_mul_u32_u24_e32 v82, s8, v158
	v_mul_u32_u24_e32 v84, s8, v159
	v_lshlrev_b32_e32 v132, 2, v2
	v_lshlrev_b32_e32 v4, 2, v4
	v_mov_b32_e32 v5, v133
	v_lshlrev_b32_e32 v10, 2, v10
	v_mov_b32_e32 v11, v133
	v_lshlrev_b32_e32 v12, 2, v12
	v_mov_b32_e32 v13, v133
	v_lshlrev_b32_e32 v18, 2, v18
	v_mov_b32_e32 v19, v133
	v_lshlrev_b32_e32 v20, 2, v20
	v_mov_b32_e32 v21, v133
	v_lshlrev_b32_e32 v26, 2, v26
	v_mov_b32_e32 v27, v133
	v_lshlrev_b32_e32 v28, 2, v28
	v_mov_b32_e32 v29, v133
	v_lshlrev_b32_e32 v34, 2, v34
	v_mov_b32_e32 v35, v133
	v_lshlrev_b32_e32 v36, 2, v36
	v_mov_b32_e32 v37, v133
	v_lshlrev_b32_e32 v50, 2, v50
	v_mov_b32_e32 v51, v133
	v_lshlrev_b32_e32 v52, 2, v52
	v_mov_b32_e32 v53, v133
	v_lshlrev_b32_e32 v66, 2, v66
	v_mov_b32_e32 v67, v133
	v_lshlrev_b32_e32 v68, 2, v68
	v_mov_b32_e32 v69, v133
	v_lshlrev_b32_e32 v82, 2, v82
	v_mov_b32_e32 v83, v133
	v_lshlrev_b32_e32 v84, 2, v84
	v_mov_b32_e32 v85, v133
	v_lshl_add_u64 v[2:3], s[6:7], 0, v[132:133]
	v_lshlrev_b32_e32 v132, 2, v130
	v_lshl_add_u64 v[4:5], s[6:7], 0, v[4:5]
	v_lshl_add_u64 v[10:11], s[6:7], 0, v[10:11]
	v_lshl_add_u64 v[12:13], s[6:7], 0, v[12:13]
	v_lshl_add_u64 v[18:19], s[6:7], 0, v[18:19]
	v_lshl_add_u64 v[20:21], s[6:7], 0, v[20:21]
	v_lshl_add_u64 v[26:27], s[6:7], 0, v[26:27]
	v_lshl_add_u64 v[28:29], s[6:7], 0, v[28:29]
	v_lshl_add_u64 v[34:35], s[6:7], 0, v[34:35]
	v_lshl_add_u64 v[36:37], s[6:7], 0, v[36:37]
	v_lshl_add_u64 v[50:51], s[6:7], 0, v[50:51]
	v_lshl_add_u64 v[52:53], s[6:7], 0, v[52:53]
	v_lshl_add_u64 v[66:67], s[6:7], 0, v[66:67]
	v_lshl_add_u64 v[68:69], s[6:7], 0, v[68:69]
	v_lshl_add_u64 v[82:83], s[6:7], 0, v[82:83]
	v_lshl_add_u64 v[84:85], s[6:7], 0, v[84:85]
	v_lshl_add_u64 v[2:3], v[2:3], 0, v[132:133]
	v_lshl_add_u64 v[6:7], v[4:5], 0, v[132:133]
	v_lshl_add_u64 v[10:11], v[10:11], 0, v[132:133]
	v_lshl_add_u64 v[14:15], v[12:13], 0, v[132:133]
	v_lshl_add_u64 v[18:19], v[18:19], 0, v[132:133]
	v_lshl_add_u64 v[22:23], v[20:21], 0, v[132:133]
	v_lshl_add_u64 v[26:27], v[26:27], 0, v[132:133]
	v_lshl_add_u64 v[30:31], v[28:29], 0, v[132:133]
	v_lshl_add_u64 v[34:35], v[34:35], 0, v[132:133]
	v_lshl_add_u64 v[38:39], v[36:37], 0, v[132:133]
	v_lshl_add_u64 v[50:51], v[50:51], 0, v[132:133]
	v_lshl_add_u64 v[54:55], v[52:53], 0, v[132:133]
	v_lshl_add_u64 v[66:67], v[66:67], 0, v[132:133]
	v_lshl_add_u64 v[70:71], v[68:69], 0, v[132:133]
	v_lshl_add_u64 v[82:83], v[82:83], 0, v[132:133]
	v_lshl_add_u64 v[86:87], v[84:85], 0, v[132:133]
	global_load_dwordx4 v[2:5], v[2:3], off nt
	s_nop 0
	global_load_dwordx4 v[6:9], v[6:7], off nt
	s_nop 0
	global_load_dwordx4 v[10:13], v[10:11], off nt
	s_nop 0
	global_load_dwordx4 v[14:17], v[14:15], off nt
	s_nop 0
	global_load_dwordx4 v[18:21], v[18:19], off nt
	s_nop 0
	global_load_dwordx4 v[22:25], v[22:23], off nt
	s_nop 0
	global_load_dwordx4 v[26:29], v[26:27], off nt
	s_nop 0
	global_load_dwordx4 v[30:33], v[30:31], off nt
	s_nop 0
	global_load_dwordx4 v[34:37], v[34:35], off nt
	s_nop 0
	global_load_dwordx4 v[38:41], v[38:39], off nt
	s_nop 0
	global_load_dwordx4 v[50:53], v[50:51], off nt
	s_nop 0
	global_load_dwordx4 v[54:57], v[54:55], off nt
	s_nop 0
	global_load_dwordx4 v[66:69], v[66:67], off nt
	s_nop 0
	global_load_dwordx4 v[70:73], v[70:71], off nt
	s_nop 0
	global_load_dwordx4 v[82:85], v[82:83], off nt
	s_nop 0
	global_load_dwordx4 v[86:89], v[86:87], off nt
	s_mov_b32 s29, s30

.LBB0_58:
	v_mul_u32_u24_e32 v42, s8, v1
	v_lshlrev_b32_e32 v132, 2, v42
	v_lshl_add_u64 v[42:43], s[6:7], 0, v[132:133]
	v_lshlrev_b32_e32 v132, 2, v130
	v_lshl_add_u64 v[58:59], v[42:43], 0, v[132:133]
	v_mul_u32_u24_e32 v42, s8, v131
	v_lshlrev_b32_e32 v42, 2, v42
	v_mov_b32_e32 v43, v133
	v_lshl_add_u64 v[42:43], s[6:7], 0, v[42:43]
	v_lshl_add_u64 v[60:61], v[42:43], 0, v[132:133]
	global_load_dwordx4 v[46:49], v[58:59], off nt
	global_load_dwordx4 v[42:45], v[60:61], off nt
	v_mul_u32_u24_e32 v58, s8, v135
	v_lshlrev_b32_e32 v58, 2, v58
	v_mov_b32_e32 v59, v133
	v_lshl_add_u64 v[58:59], s[6:7], 0, v[58:59]
	v_lshl_add_u64 v[74:75], v[58:59], 0, v[132:133]
	v_mul_u32_u24_e32 v58, s8, v139
	v_lshlrev_b32_e32 v58, 2, v58
	v_mov_b32_e32 v59, v133
	v_lshl_add_u64 v[58:59], s[6:7], 0, v[58:59]
	v_lshl_add_u64 v[76:77], v[58:59], 0, v[132:133]
	global_load_dwordx4 v[62:65], v[74:75], off nt
	global_load_dwordx4 v[58:61], v[76:77], off nt
	v_mul_u32_u24_e32 v74, s8, v141
	v_lshlrev_b32_e32 v74, 2, v74
	v_mov_b32_e32 v75, v133
	v_lshl_add_u64 v[74:75], s[6:7], 0, v[74:75]
	v_lshl_add_u64 v[90:91], v[74:75], 0, v[132:133]
	v_mul_u32_u24_e32 v74, s8, v143
	v_lshlrev_b32_e32 v74, 2, v74
	v_mov_b32_e32 v75, v133
	v_lshl_add_u64 v[74:75], s[6:7], 0, v[74:75]
	v_lshl_add_u64 v[92:93], v[74:75], 0, v[132:133]
	global_load_dwordx4 v[78:81], v[90:91], off nt
	global_load_dwordx4 v[74:77], v[92:93], off nt
	v_mul_u32_u24_e32 v90, s8, v145
	v_mul_u32_u24_e32 v92, s8, v147
	v_mul_u32_u24_e32 v98, s8, v149
	v_mul_u32_u24_e32 v100, s8, v151
	v_mul_u32_u24_e32 v106, s8, v154
	v_mul_u32_u24_e32 v108, s8, v155
	v_mul_u32_u24_e32 v114, s8, v156
	v_mul_u32_u24_e32 v116, s8, v157
	v_mul_u32_u24_e32 v122, s8, v158
	v_mul_u32_u24_e32 v124, s8, v159
	v_lshlrev_b32_e32 v90, 2, v90
	v_mov_b32_e32 v91, v133
	v_lshlrev_b32_e32 v92, 2, v92
	v_mov_b32_e32 v93, v133
	v_lshlrev_b32_e32 v98, 2, v98
	v_mov_b32_e32 v99, v133
	v_lshlrev_b32_e32 v100, 2, v100
	v_mov_b32_e32 v101, v133
	v_lshlrev_b32_e32 v106, 2, v106
	v_mov_b32_e32 v107, v133
	v_lshlrev_b32_e32 v108, 2, v108
	v_mov_b32_e32 v109, v133
	v_lshlrev_b32_e32 v114, 2, v114
	v_mov_b32_e32 v115, v133
	v_lshlrev_b32_e32 v116, 2, v116
	v_mov_b32_e32 v117, v133
	v_lshlrev_b32_e32 v122, 2, v122
	v_mov_b32_e32 v123, v133
	v_lshlrev_b32_e32 v124, 2, v124
	v_mov_b32_e32 v125, v133
	v_lshl_add_u64 v[90:91], s[6:7], 0, v[90:91]
	v_lshl_add_u64 v[92:93], s[6:7], 0, v[92:93]
	v_lshl_add_u64 v[98:99], s[6:7], 0, v[98:99]
	v_lshl_add_u64 v[100:101], s[6:7], 0, v[100:101]
	v_lshl_add_u64 v[106:107], s[6:7], 0, v[106:107]
	v_lshl_add_u64 v[108:109], s[6:7], 0, v[108:109]
	v_lshl_add_u64 v[114:115], s[6:7], 0, v[114:115]
	v_lshl_add_u64 v[116:117], s[6:7], 0, v[116:117]
	v_lshl_add_u64 v[122:123], s[6:7], 0, v[122:123]
	v_lshl_add_u64 v[124:125], s[6:7], 0, v[124:125]
	v_lshl_add_u64 v[90:91], v[90:91], 0, v[132:133]
	v_lshl_add_u64 v[92:93], v[92:93], 0, v[132:133]
	v_lshl_add_u64 v[98:99], v[98:99], 0, v[132:133]
	v_lshl_add_u64 v[100:101], v[100:101], 0, v[132:133]
	v_lshl_add_u64 v[106:107], v[106:107], 0, v[132:133]
	v_lshl_add_u64 v[108:109], v[108:109], 0, v[132:133]
	v_lshl_add_u64 v[114:115], v[114:115], 0, v[132:133]
	v_lshl_add_u64 v[116:117], v[116:117], 0, v[132:133]
	v_lshl_add_u64 v[122:123], v[122:123], 0, v[132:133]
	v_lshl_add_u64 v[124:125], v[124:125], 0, v[132:133]
	global_load_dwordx4 v[94:97], v[90:91], off nt
	s_nop 0
	global_load_dwordx4 v[90:93], v[92:93], off nt
	s_nop 0
	global_load_dwordx4 v[102:105], v[98:99], off nt
	s_nop 0
	global_load_dwordx4 v[98:101], v[100:101], off nt
	s_nop 0
	global_load_dwordx4 v[110:113], v[106:107], off nt
	s_nop 0
	global_load_dwordx4 v[106:109], v[108:109], off nt
	s_nop 0
	global_load_dwordx4 v[118:121], v[114:115], off nt
	s_nop 0
	global_load_dwordx4 v[114:117], v[116:117], off nt
	s_nop 0
	global_load_dwordx4 v[126:129], v[122:123], off nt
	s_nop 0
	global_load_dwordx4 v[122:125], v[124:125], off nt
